# prologue pre-norm loop: gain/scale/shift vectors loaded once per 4-token group (same modulation row) into free VGPRs and reused; 36 reloads and their waits removed
# baseline (speedup 1.0000x reference)
; DEV float fast_rsq(float x) { return __builtin_amdgcn_rsqf(x); }
; DEV void norm_store(const Params& p, int tok, const float (&xv)[2][8], const float* __restrict__ gain, const float* __restrict__ sh, const float* __restrict__ scl, bool with_lo, int lane) {
;     float ss = 0.f;
; #pragma unroll
;     for (int j = 0; j < 2; ++j)
; #pragma unroll
;         for (int i = 0; i < 8; ++i) ss += xv[j][i] * xv[j][i];
;     ss = wave_sum(ss);
;     const float rinv = fast_rsq(ss * (1.0f / 1024.0f) + EPS);
;     bf16_t* H = (bf16_t*)(p.ws + WS_H) + (size_t)tok * HLD;
; #pragma unroll
;     for (int j = 0; j < 2; ++j) { const int col = 8 * lane + 512 * j; float y[8];
;         const f32x4 g0 = *(const f32x4*)(gain + col), g1 = *(const f32x4*)(gain + col + 4), s0 = *(const f32x4*)(scl + col), s1 = *(const f32x4*)(scl + col + 4), h0 = *(const f32x4*)(sh + col), h1 = *(const f32x4*)(sh + col + 4);
; #pragma unroll
;         for (int i = 0; i < 4; ++i) { y[i] = xv[j][i] * rinv * g0[i] * (1.0f + s0[i]) + h0[i]; y[4 + i] = xv[j][4 + i] * rinv * g1[i] * (1.0f + s1[i]) + h1[i]; }
;         if (!with_lo) { const u32x4 w = {cvtpk(y[0], y[1]), cvtpk(y[2], y[3]), cvtpk(y[4], y[5]), cvtpk(y[6], y[7])}; *(u32x4*)(H + col) = w; }
;         else { *(u32x2*)((unsigned char*)H + col) = (u32x2){pk_fp8x4(y[0], y[1], y[2], y[3]), pk_fp8x4(y[4], y[5], y[6], y[7])};
;             const u32x4 wl = {cvtpk_h(y[0], y[1]), cvtpk_h(y[2], y[3]), cvtpk_h(y[4], y[5]), cvtpk_h(y[6], y[7])};
;             *(u32x4*)(H + 1024 + col) = wl; } }
; }
; DEV void phase_norm(const Params& p, int layer, int which) {
;     ...
;     for (int tok0 = gw * 4; tok0 < ntok; tok0 += nw * 4) {
;         float xv[4][2][8];
; #pragma unroll
;         for (int q = 0; q < 4; ++q) { const int tok = tok0 + q;
;             if (which == 0 && layer == 0) load_row(tok < NLAT ? p.x + (size_t)tok * 1024 : p.ctx + (size_t)(tok - NLAT) * 1024, xv[q], lane);
;             else load_row_bf((const bf16_t*)(p.ws + WS_X) + (size_t)tok * 1024, xv[q], lane); }
; #pragma unroll
;         for (int q = 0; q < 4; ++q) { const int tok = tok0 + q; const float* m = mod + mod_row(tok) * 6144;
;             if (which == 0) norm_store(p, tok, xv[q], p.norm_mix + layer * 1024, m, m + 1024, false, lane);
;             else norm_store(p, tok, xv[q], p.norm_ffn + layer * 1024, m + 3072, m + 4096, true, lane); }
.LBB0_137:
	s_or_b64 exec, exec, s[12:13]
	s_waitcnt vmcnt(10)
	v_mul_f32_e32 v0, v63, v63
	v_fmac_f32_e32 v0, v62, v62
	v_fmac_f32_e32 v0, v64, v64
	v_fmac_f32_e32 v0, v65, v65
	v_fmac_f32_e32 v0, v58, v58
	v_fmac_f32_e32 v0, v59, v59
	v_fmac_f32_e32 v0, v60, v60
	v_fmac_f32_e32 v0, v61, v61
	s_waitcnt vmcnt(8)
	v_fmac_f32_e32 v0, v54, v54
	v_fmac_f32_e32 v0, v55, v55
	v_fmac_f32_e32 v0, v56, v56
	v_min_i32_e32 v85, 0x8000, v66
	v_fmac_f32_e32 v0, v57, v57
	v_ashrrev_i32_e32 v85, 14, v85
	v_fmac_f32_e32 v0, v50, v50
	v_mul_i32_i24_e32 v94, 0x1800, v85
	v_fmac_f32_e32 v0, v51, v51
	v_ashrrev_i32_e32 v95, 31, v94
	v_fmac_f32_e32 v0, v52, v52
	v_lshl_add_u64 v[106:107], v[94:95], 2, s[4:5]
	v_fmac_f32_e32 v0, v53, v53
	v_lshl_add_u64 v[114:115], v[106:107], 0, s[10:11]
	v_lshl_add_u64 v[90:91], v[2:3], 0, v[68:69]
	v_mov_b32_e32 v81, v0
	v_lshl_add_u64 v[108:109], v[114:115], 0, v[68:69]
	global_load_dwordx4 v[10:13], v[90:91], off offset:16
	global_load_dwordx4 v[14:17], v[90:91], off
	global_load_dwordx4 v[2:5], v[90:91], off offset:2064
	global_load_dwordx4 v[6:9], v[90:91], off offset:2048
	s_nop 1
	v_permlane32_swap_b32 v0, v81
	s_nop 1
	global_load_dwordx4 v[148:151], v[70:71], off
	global_load_dwordx4 v[156:159], v[108:109], off
	global_load_dwordx4 v[152:155], v[70:71], off offset:16
	global_load_dwordx4 v[166:169], v[108:109], off offset:16
	v_lshl_add_u64 v[116:117], v[106:107], 0, v[68:69]
	global_load_dwordx4 v[170:173], v[116:117], off
	global_load_dwordx4 v[174:177], v[116:117], off offset:16
	v_add_f32_e32 v0, v0, v81
	ds_swizzle_b32 v81, v0 offset:swizzle(SWAP,16)
	v_add_co_u32_e32 v118, vcc, s17, v78
	s_waitcnt vmcnt(16)
	v_mul_f32_e32 v85, v47, v47
	v_addc_co_u32_e32 v119, vcc, -1, v79, vcc
	s_waitcnt lgkmcnt(0)
	v_add_f32_e32 v0, v0, v81
	v_mov_b32_e32 v81, v69
	v_fmac_f32_e32 v85, v46, v46
	v_add_f32_dpp v0, v0, v0 row_ror:8 row_mask:0xf bank_mask:0xf bound_ctrl:1
	v_fmac_f32_e32 v85, v48, v48
	v_fmac_f32_e32 v85, v49, v49
	v_add_f32_dpp v0, v0, v0 row_ror:4 row_mask:0xf bank_mask:0xf bound_ctrl:1
	v_fmac_f32_e32 v85, v42, v42
	v_fmac_f32_e32 v85, v43, v43
	v_add_f32_dpp v0, v0, v0 quad_perm:[2,3,0,1] row_mask:0xf bank_mask:0xf bound_ctrl:1
	v_fmac_f32_e32 v85, v44, v44
	v_fmac_f32_e32 v85, v45, v45
	v_add_f32_dpp v0, v0, v0 quad_perm:[1,0,3,2] row_mask:0xf bank_mask:0xf bound_ctrl:1
	v_fmamk_f32 v0, v0, 0x3a800000, v88
	v_rsq_f32_e32 v0, v0
	s_waitcnt vmcnt(14)
	v_fmac_f32_e32 v85, v38, v38
	v_fmac_f32_e32 v85, v39, v39
	v_min_i32_e32 v89, 0x8000, v74
	v_pk_mul_f32 v[62:63], v[62:63], v[0:1] op_sel_hi:[1,0]
	v_pk_mul_f32 v[64:65], v[64:65], v[0:1] op_sel_hi:[1,0]
	v_pk_mul_f32 v[58:59], v[58:59], v[0:1] op_sel_hi:[1,0]
	v_pk_mul_f32 v[60:61], v[60:61], v[0:1] op_sel_hi:[1,0]
	v_fmac_f32_e32 v85, v40, v40
	v_ashrrev_i32_e32 v89, 14, v89
	v_fmac_f32_e32 v85, v41, v41
	v_fmac_f32_e32 v85, v34, v34
	v_fmac_f32_e32 v85, v35, v35
	v_pk_mul_f32 v[54:55], v[54:55], v[0:1] op_sel_hi:[1,0]
	v_pk_mul_f32 v[56:57], v[56:57], v[0:1] op_sel_hi:[1,0]
	v_pk_mul_f32 v[50:51], v[50:51], v[0:1] op_sel_hi:[1,0]
	v_pk_mul_f32 v[52:53], v[52:53], v[0:1] op_sel_hi:[1,0]
	v_fmac_f32_e32 v85, v36, v36
	v_fmac_f32_e32 v85, v37, v37
	v_min_i32_e32 v84, 0x8000, v84
	v_ashrrev_i32_e32 v84, 14, v84
	v_mul_i32_i24_e32 v84, 0x1800, v84
	v_add_u32_e32 v66, s6, v66
	v_lshl_add_u64 v[74:75], v[74:75], 0, s[6:7]
	v_lshl_add_u64 v[76:77], v[76:77], 0, s[8:9]
	s_waitcnt vmcnt(3)
	v_pk_mul_f32 v[58:59], v[152:153], v[58:59]
	v_pk_mul_f32 v[62:63], v[148:149], v[62:63]
	v_pk_mul_f32 v[64:65], v[150:151], v[64:65]
	v_pk_add_f32 v[90:91], v[156:157], 1.0 op_sel_hi:[1,0]
	v_pk_add_f32 v[92:93], v[158:159], 1.0 op_sel_hi:[1,0]
	v_pk_mul_f32 v[60:61], v[154:155], v[60:61]
	s_waitcnt vmcnt(2)
	v_pk_add_f32 v[94:95], v[166:167], 1.0 op_sel_hi:[1,0]
	v_pk_add_f32 v[96:97], v[168:169], 1.0 op_sel_hi:[1,0]
	s_waitcnt vmcnt(1)
	v_pk_fma_f32 v[62:63], v[90:91], v[62:63], v[170:171]
	v_pk_fma_f32 v[64:65], v[92:93], v[64:65], v[172:173]
	s_waitcnt vmcnt(0)
	v_pk_fma_f32 v[90:91], v[94:95], v[58:59], v[174:175]
	v_pk_fma_f32 v[92:93], v[96:97], v[60:61], v[176:177]
	v_cvt_pk_bf16_f32 v58, v62, v63
	v_cvt_pk_bf16_f32 v59, v64, v65
	v_cvt_pk_bf16_f32 v60, v90, v91
	v_cvt_pk_bf16_f32 v61, v92, v93
	global_store_dwordx4 v[118:119], v[58:61], off offset:-1280
	global_load_dwordx4 v[180:183], v[70:71], off offset:2048
	v_lshl_add_u64 v[106:107], v[114:115], 0, v[80:81]
	global_load_dwordx4 v[202:205], v[106:107], off
	global_load_dwordx4 v[198:201], v[70:71], off offset:2064
	global_load_dwordx4 v[210:213], v[106:107], off offset:16
	global_load_dwordx4 v[214:217], v[116:117], off offset:2048
	global_load_dwordx4 v[228:231], v[116:117], off offset:2064
	v_mul_i32_i24_e32 v106, 0x1800, v89
	v_ashrrev_i32_e32 v107, 31, v106
	v_lshl_add_u64 v[106:107], v[106:107], 2, s[4:5]
	v_lshl_add_u64 v[108:109], v[106:107], 0, s[10:11]
	v_mov_b32_e32 v89, v85
	s_waitcnt vmcnt(3)
	v_pk_mul_f32 v[50:51], v[50:51], v[198:199]
	v_pk_mul_f32 v[54:55], v[54:55], v[180:181]
	v_pk_mul_f32 v[56:57], v[56:57], v[182:183]
	v_pk_add_f32 v[58:59], v[202:203], 1.0 op_sel_hi:[1,0]
	v_pk_add_f32 v[60:61], v[204:205], 1.0 op_sel_hi:[1,0]
	v_pk_mul_f32 v[52:53], v[52:53], v[200:201]
	s_waitcnt vmcnt(2)
	v_pk_add_f32 v[62:63], v[210:211], 1.0 op_sel_hi:[1,0]
	v_pk_add_f32 v[64:65], v[212:213], 1.0 op_sel_hi:[1,0]
	s_waitcnt vmcnt(1)
	v_pk_fma_f32 v[54:55], v[54:55], v[58:59], v[214:215]
	v_pk_fma_f32 v[56:57], v[56:57], v[60:61], v[216:217]
	s_waitcnt vmcnt(0)
; DEV unsigned cvtpk(float lo, float hi) { f32x2 v = {lo, hi}; bf16v2 r = __builtin_convertvector(v, bf16v2); return __builtin_bit_cast(unsigned, r); }
; DEV unsigned cvtpk_h(float lo, float hi) { f32x2 v = {lo, hi}; f16x2 r = __builtin_convertvector(v, f16x2); return __builtin_bit_cast(unsigned, r); }
; DEV unsigned pk_fp8x4(float a, float b, float c, float d) { int w = __builtin_amdgcn_cvt_pk_fp8_f32(a, b, 0, false); w = __builtin_amdgcn_cvt_pk_fp8_f32(c, d, w, true); return (unsigned)w; }
; DEV void norm_store(const Params& p, int tok, const float (&xv)[2][8], const float* __restrict__ gain, const float* __restrict__ sh, const float* __restrict__ scl, bool with_lo, int lane) {
;     ...
;     for (int j = 0; j < 2; ++j) { const int col = 8 * lane + 512 * j; float y[8];
;         const f32x4 g0 = *(const f32x4*)(gain + col), g1 = *(const f32x4*)(gain + col + 4), s0 = *(const f32x4*)(scl + col), s1 = *(const f32x4*)(scl + col + 4), h0 = *(const f32x4*)(sh + col), h1 = *(const f32x4*)(sh + col + 4);
; #pragma unroll
;         for (int i = 0; i < 4; ++i) { y[i] = xv[j][i] * rinv * g0[i] * (1.0f + s0[i]) + h0[i]; y[4 + i] = xv[j][4 + i] * rinv * g1[i] * (1.0f + s1[i]) + h1[i]; }
;         if (!with_lo) { const u32x4 w = {cvtpk(y[0], y[1]), cvtpk(y[2], y[3]), cvtpk(y[4], y[5]), cvtpk(y[6], y[7])}; *(u32x4*)(H + col) = w; }
;         else { *(u32x2*)((unsigned char*)H + col) = (u32x2){pk_fp8x4(y[0], y[1], y[2], y[3]), pk_fp8x4(y[4], y[5], y[6], y[7])};
;             const u32x4 wl = {cvtpk_h(y[0], y[1]), cvtpk_h(y[2], y[3]), cvtpk_h(y[4], y[5]), cvtpk_h(y[6], y[7])};
;             *(u32x4*)(H + 1024 + col) = wl; } }
	v_pk_fma_f32 v[58:59], v[50:51], v[62:63], v[228:229]
	v_pk_fma_f32 v[60:61], v[52:53], v[64:65], v[230:231]
	v_cvt_pk_bf16_f32 v50, v54, v55
	v_cvt_pk_bf16_f32 v51, v56, v57
	v_cvt_pk_bf16_f32 v52, v58, v59
	v_cvt_pk_bf16_f32 v53, v60, v61
	v_lshl_add_u64 v[90:91], v[108:109], 0, v[68:69]
	global_store_dwordx4 v[118:119], v[50:53], off offset:-256
	s_nop 1
	v_permlane32_swap_b32 v85, v89
	s_nop 1
	v_lshl_add_u64 v[98:99], v[106:107], 0, v[68:69]
	v_add_f32_e32 v0, v85, v89
	ds_swizzle_b32 v85, v0 offset:swizzle(SWAP,16)
	v_add_co_u32_e32 v100, vcc, s18, v78
	v_mul_f32_e32 v89, v31, v31
	s_nop 0
	v_addc_co_u32_e32 v101, vcc, -1, v79, vcc
	s_waitcnt lgkmcnt(0)
	v_add_f32_e32 v0, v0, v85
	v_fmac_f32_e32 v89, v30, v30
	v_fmac_f32_e32 v89, v32, v32
	v_add_f32_dpp v0, v0, v0 row_ror:8 row_mask:0xf bank_mask:0xf bound_ctrl:1
	v_fmac_f32_e32 v89, v33, v33
	v_fmac_f32_e32 v89, v26, v26
	v_add_f32_dpp v0, v0, v0 row_ror:4 row_mask:0xf bank_mask:0xf bound_ctrl:1
	v_fmac_f32_e32 v89, v27, v27
	v_fmac_f32_e32 v89, v28, v28
	v_add_f32_dpp v0, v0, v0 quad_perm:[2,3,0,1] row_mask:0xf bank_mask:0xf bound_ctrl:1
	v_fmac_f32_e32 v89, v29, v29
	v_fmac_f32_e32 v89, v22, v22
	v_add_f32_dpp v0, v0, v0 quad_perm:[1,0,3,2] row_mask:0xf bank_mask:0xf bound_ctrl:1
	v_fmamk_f32 v0, v0, 0x3a800000, v88
	v_rsq_f32_e32 v0, v0
	v_fmac_f32_e32 v89, v23, v23
	v_fmac_f32_e32 v89, v24, v24
	v_fmac_f32_e32 v89, v25, v25
	v_pk_mul_f32 v[46:47], v[46:47], v[0:1] op_sel_hi:[1,0]
	v_pk_mul_f32 v[48:49], v[48:49], v[0:1] op_sel_hi:[1,0]
	v_pk_mul_f32 v[42:43], v[42:43], v[0:1] op_sel_hi:[1,0]
	v_pk_mul_f32 v[44:45], v[44:45], v[0:1] op_sel_hi:[1,0]
	v_fmac_f32_e32 v89, v18, v18
	v_ashrrev_i32_e32 v85, 31, v84
	v_fmac_f32_e32 v89, v19, v19
	v_pk_mul_f32 v[38:39], v[38:39], v[0:1] op_sel_hi:[1,0]
	v_pk_mul_f32 v[40:41], v[40:41], v[0:1] op_sel_hi:[1,0]
	v_pk_mul_f32 v[34:35], v[34:35], v[0:1] op_sel_hi:[1,0]
	v_pk_mul_f32 v[36:37], v[36:37], v[0:1] op_sel_hi:[1,0]
	v_lshl_add_u64 v[84:85], v[84:85], 2, s[4:5]
	v_fmac_f32_e32 v89, v20, v20
	v_fmac_f32_e32 v89, v21, v21
	v_cmp_lt_i32_e32 vcc, s19, v66
	s_or_b64 s[0:1], vcc, s[0:1]
	v_pk_mul_f32 v[46:47], v[148:149], v[46:47]
	v_pk_mul_f32 v[48:49], v[150:151], v[48:49]
	v_pk_add_f32 v[50:51], v[156:157], 1.0 op_sel_hi:[1,0]
	v_pk_add_f32 v[52:53], v[158:159], 1.0 op_sel_hi:[1,0]
	v_pk_mul_f32 v[42:43], v[152:153], v[42:43]
	v_pk_mul_f32 v[44:45], v[154:155], v[44:45]
	v_pk_add_f32 v[54:55], v[166:167], 1.0 op_sel_hi:[1,0]
	v_pk_add_f32 v[56:57], v[168:169], 1.0 op_sel_hi:[1,0]
	v_pk_fma_f32 v[46:47], v[50:51], v[46:47], v[170:171]
	v_pk_fma_f32 v[48:49], v[52:53], v[48:49], v[172:173]
	v_pk_fma_f32 v[50:51], v[54:55], v[42:43], v[174:175]
	v_pk_fma_f32 v[52:53], v[56:57], v[44:45], v[176:177]
	v_cvt_pk_bf16_f32 v42, v46, v47
	v_cvt_pk_bf16_f32 v43, v48, v49
	v_cvt_pk_bf16_f32 v44, v50, v51
	v_cvt_pk_bf16_f32 v45, v52, v53
	global_store_dwordx4 v[100:101], v[42:45], off offset:-1152
	v_lshl_add_u64 v[90:91], v[108:109], 0, v[80:81]
	v_mov_b32_e32 v90, v89
	v_pk_mul_f32 v[34:35], v[34:35], v[198:199]
	v_pk_mul_f32 v[38:39], v[38:39], v[180:181]
	v_pk_mul_f32 v[40:41], v[40:41], v[182:183]
	v_pk_add_f32 v[42:43], v[202:203], 1.0 op_sel_hi:[1,0]
	v_pk_add_f32 v[44:45], v[204:205], 1.0 op_sel_hi:[1,0]
	v_pk_mul_f32 v[36:37], v[36:37], v[200:201]
	v_pk_add_f32 v[46:47], v[210:211], 1.0 op_sel_hi:[1,0]
	v_pk_add_f32 v[48:49], v[212:213], 1.0 op_sel_hi:[1,0]
	v_pk_fma_f32 v[38:39], v[38:39], v[42:43], v[214:215]
	v_pk_fma_f32 v[40:41], v[40:41], v[44:45], v[216:217]
	v_pk_fma_f32 v[42:43], v[34:35], v[46:47], v[228:229]
	v_pk_fma_f32 v[44:45], v[36:37], v[48:49], v[230:231]
	v_lshl_add_u64 v[58:59], v[84:85], 0, s[10:11]
	v_cvt_pk_bf16_f32 v34, v38, v39
	v_cvt_pk_bf16_f32 v35, v40, v41
	v_cvt_pk_bf16_f32 v36, v42, v43
	v_cvt_pk_bf16_f32 v37, v44, v45
	v_lshl_add_u64 v[50:51], v[58:59], 0, v[68:69]
	global_store_dwordx4 v[100:101], v[34:37], off offset:-128
	s_nop 1
	v_permlane32_swap_b32 v89, v90
	s_nop 1
	v_lshl_add_u64 v[60:61], v[84:85], 0, v[68:69]
	v_add_f32_e32 v0, v89, v90
	ds_swizzle_b32 v62, v0 offset:swizzle(SWAP,16)
	s_waitcnt lgkmcnt(0)
; DEV unsigned cvtpk(float lo, float hi) { f32x2 v = {lo, hi}; bf16v2 r = __builtin_convertvector(v, bf16v2); return __builtin_bit_cast(unsigned, r); }
; DEV unsigned cvtpk_h(float lo, float hi) { f32x2 v = {lo, hi}; f16x2 r = __builtin_convertvector(v, f16x2); return __builtin_bit_cast(unsigned, r); }
; DEV unsigned pk_fp8x4(float a, float b, float c, float d) { int w = __builtin_amdgcn_cvt_pk_fp8_f32(a, b, 0, false); w = __builtin_amdgcn_cvt_pk_fp8_f32(c, d, w, true); return (unsigned)w; }
; DEV void norm_store(const Params& p, int tok, const float (&xv)[2][8], const float* __restrict__ gain, const float* __restrict__ sh, const float* __restrict__ scl, bool with_lo, int lane) {
;     ...
;     for (int j = 0; j < 2; ++j) { const int col = 8 * lane + 512 * j; float y[8];
;         const f32x4 g0 = *(const f32x4*)(gain + col), g1 = *(const f32x4*)(gain + col + 4), s0 = *(const f32x4*)(scl + col), s1 = *(const f32x4*)(scl + col + 4), h0 = *(const f32x4*)(sh + col), h1 = *(const f32x4*)(sh + col + 4);
; #pragma unroll
;         for (int i = 0; i < 4; ++i) { y[i] = xv[j][i] * rinv * g0[i] * (1.0f + s0[i]) + h0[i]; y[4 + i] = xv[j][4 + i] * rinv * g1[i] * (1.0f + s1[i]) + h1[i]; }
;         if (!with_lo) { const u32x4 w = {cvtpk(y[0], y[1]), cvtpk(y[2], y[3]), cvtpk(y[4], y[5]), cvtpk(y[6], y[7])}; *(u32x4*)(H + col) = w; }
;         else { *(u32x2*)((unsigned char*)H + col) = (u32x2){pk_fp8x4(y[0], y[1], y[2], y[3]), pk_fp8x4(y[4], y[5], y[6], y[7])};
;             const u32x4 wl = {cvtpk_h(y[0], y[1]), cvtpk_h(y[2], y[3]), cvtpk_h(y[4], y[5]), cvtpk_h(y[6], y[7])};
;             *(u32x4*)(H + 1024 + col) = wl; } }
	v_add_f32_e32 v0, v0, v62
	s_nop 1
	v_add_f32_dpp v0, v0, v0 row_ror:8 row_mask:0xf bank_mask:0xf bound_ctrl:1
	s_nop 1
	v_add_f32_dpp v0, v0, v0 row_ror:4 row_mask:0xf bank_mask:0xf bound_ctrl:1
	s_nop 1
	v_add_f32_dpp v0, v0, v0 quad_perm:[2,3,0,1] row_mask:0xf bank_mask:0xf bound_ctrl:1
	s_nop 1
	v_add_f32_dpp v0, v0, v0 quad_perm:[1,0,3,2] row_mask:0xf bank_mask:0xf bound_ctrl:1
	v_fmamk_f32 v0, v0, 0x3a800000, v88
	v_rsq_f32_e32 v0, v0
	s_nop 0
	v_pk_mul_f32 v[30:31], v[30:31], v[0:1] op_sel_hi:[1,0]
	v_pk_mul_f32 v[32:33], v[32:33], v[0:1] op_sel_hi:[1,0]
	v_pk_mul_f32 v[26:27], v[26:27], v[0:1] op_sel_hi:[1,0]
	v_pk_mul_f32 v[28:29], v[28:29], v[0:1] op_sel_hi:[1,0]
	v_pk_mul_f32 v[22:23], v[22:23], v[0:1] op_sel_hi:[1,0]
	v_pk_mul_f32 v[24:25], v[24:25], v[0:1] op_sel_hi:[1,0]
	v_pk_mul_f32 v[18:19], v[18:19], v[0:1] op_sel_hi:[1,0]
	v_pk_mul_f32 v[20:21], v[20:21], v[0:1] op_sel_hi:[1,0]
	v_pk_mul_f32 v[30:31], v[148:149], v[30:31]
	v_pk_mul_f32 v[26:27], v[152:153], v[26:27]
	v_pk_mul_f32 v[32:33], v[150:151], v[32:33]
	v_pk_mul_f32 v[28:29], v[154:155], v[28:29]
	v_pk_add_f32 v[34:35], v[156:157], 1.0 op_sel_hi:[1,0]
	v_pk_add_f32 v[36:37], v[158:159], 1.0 op_sel_hi:[1,0]
	v_pk_add_f32 v[38:39], v[166:167], 1.0 op_sel_hi:[1,0]
	v_pk_add_f32 v[40:41], v[168:169], 1.0 op_sel_hi:[1,0]
	v_pk_fma_f32 v[30:31], v[34:35], v[30:31], v[170:171]
	v_pk_fma_f32 v[34:35], v[38:39], v[26:27], v[174:175]
	v_pk_fma_f32 v[32:33], v[36:37], v[32:33], v[172:173]
	v_pk_fma_f32 v[36:37], v[40:41], v[28:29], v[176:177]
	v_cvt_pk_bf16_f32 v26, v30, v31
	v_cvt_pk_bf16_f32 v27, v32, v33
	v_cvt_pk_bf16_f32 v28, v34, v35
	v_cvt_pk_bf16_f32 v29, v36, v37
	global_store_dwordx4 v[78:79], v[26:29], off offset:-1024
	v_lshl_add_u64 v[50:51], v[58:59], 0, v[80:81]
	v_mul_f32_e32 v56, v15, v15
	v_fmac_f32_e32 v56, v14, v14
	v_fmac_f32_e32 v56, v16, v16
	v_fmac_f32_e32 v56, v17, v17
	v_fmac_f32_e32 v56, v10, v10
	v_fmac_f32_e32 v56, v11, v11
	v_fmac_f32_e32 v56, v12, v12
	v_fmac_f32_e32 v56, v13, v13
	v_fmac_f32_e32 v56, v6, v6
	v_fmac_f32_e32 v56, v7, v7
	v_fmac_f32_e32 v56, v8, v8
	v_min_i32_e32 v50, 0x8000, v82
	v_fmac_f32_e32 v56, v9, v9
	v_ashrrev_i32_e32 v50, 14, v50
	v_fmac_f32_e32 v56, v2, v2
	v_mul_i32_i24_e32 v50, 0x1800, v50
	v_fmac_f32_e32 v56, v3, v3
	v_ashrrev_i32_e32 v51, 31, v50
	v_fmac_f32_e32 v56, v4, v4
	v_lshl_add_u64 v[50:51], v[50:51], 2, s[4:5]
	v_fmac_f32_e32 v56, v5, v5
	v_lshl_add_u64 v[52:53], v[50:51], 0, s[10:11]
	v_mov_b32_e32 v57, v56
	v_lshl_add_u64 v[54:55], v[52:53], 0, v[68:69]
	v_pk_mul_f32 v[18:19], v[18:19], v[198:199]
	v_pk_mul_f32 v[22:23], v[22:23], v[180:181]
	v_pk_mul_f32 v[24:25], v[24:25], v[182:183]
	v_pk_add_f32 v[26:27], v[202:203], 1.0 op_sel_hi:[1,0]
	v_pk_add_f32 v[28:29], v[210:211], 1.0 op_sel_hi:[1,0]
	v_pk_add_f32 v[30:31], v[204:205], 1.0 op_sel_hi:[1,0]
	v_pk_mul_f32 v[20:21], v[20:21], v[200:201]
	v_pk_add_f32 v[32:33], v[212:213], 1.0 op_sel_hi:[1,0]
	v_pk_fma_f32 v[22:23], v[22:23], v[26:27], v[214:215]
	v_pk_fma_f32 v[26:27], v[18:19], v[28:29], v[228:229]
	v_pk_fma_f32 v[24:25], v[24:25], v[30:31], v[216:217]
	v_pk_fma_f32 v[28:29], v[20:21], v[32:33], v[230:231]
	v_cvt_pk_bf16_f32 v18, v22, v23
	v_cvt_pk_bf16_f32 v19, v24, v25
	v_cvt_pk_bf16_f32 v20, v26, v27
	v_cvt_pk_bf16_f32 v21, v28, v29
	global_store_dwordx4 v[78:79], v[18:21], off
	s_nop 1
	v_permlane32_swap_b32 v56, v57
	s_nop 1
	v_lshl_add_u64 v[42:43], v[50:51], 0, v[68:69]
	v_add_f32_e32 v46, v56, v57
	ds_swizzle_b32 v47, v46 offset:swizzle(SWAP,16)
	v_mad_u64_u32 v[44:45], s[12:13], v82, s14, v[72:73]
	v_mov_b32_e32 v0, v45
	v_mad_u64_u32 v[48:49], s[12:13], v83, s14, v[0:1]
	s_waitcnt lgkmcnt(0)
	v_add_f32_e32 v45, v46, v47
	v_readlane_b32 s12, v252, 7
	v_readlane_b32 s13, v252, 8
	v_add_f32_dpp v45, v45, v45 row_ror:8 row_mask:0xf bank_mask:0xf bound_ctrl:1
	s_nop 0
	v_lshl_add_u64 v[78:79], v[78:79], 0, s[12:13]
	v_add_f32_dpp v45, v45, v45 row_ror:4 row_mask:0xf bank_mask:0xf bound_ctrl:1
	s_nop 1
	v_add_f32_dpp v45, v45, v45 quad_perm:[2,3,0,1] row_mask:0xf bank_mask:0xf bound_ctrl:1
	s_nop 1
	v_add_f32_dpp v45, v45, v45 quad_perm:[1,0,3,2] row_mask:0xf bank_mask:0xf bound_ctrl:1
	v_fmamk_f32 v45, v45, 0x3a800000, v88
	v_rsq_f32_e32 v46, v45
	v_mov_b32_e32 v45, v48
	v_lshl_add_u64 v[48:49], v[52:53], 0, v[80:81]
	v_pk_mul_f32 v[14:15], v[14:15], v[46:47] op_sel_hi:[1,0]
	v_pk_mul_f32 v[10:11], v[10:11], v[46:47] op_sel_hi:[1,0]
	v_pk_mul_f32 v[16:17], v[16:17], v[46:47] op_sel_hi:[1,0]
	v_pk_mul_f32 v[12:13], v[12:13], v[46:47] op_sel_hi:[1,0]
	v_pk_mul_f32 v[6:7], v[6:7], v[46:47] op_sel_hi:[1,0]
	v_pk_mul_f32 v[2:3], v[2:3], v[46:47] op_sel_hi:[1,0]
	v_pk_mul_f32 v[8:9], v[8:9], v[46:47] op_sel_hi:[1,0]
	v_pk_mul_f32 v[4:5], v[4:5], v[46:47] op_sel_hi:[1,0]
	v_pk_mul_f32 v[14:15], v[148:149], v[14:15]
	v_pk_add_f32 v[18:19], v[156:157], 1.0 op_sel_hi:[1,0]
	v_pk_mul_f32 v[10:11], v[152:153], v[10:11]
	v_pk_add_f32 v[22:23], v[166:167], 1.0 op_sel_hi:[1,0]
	v_pk_mul_f32 v[16:17], v[150:151], v[16:17]
	v_pk_add_f32 v[20:21], v[158:159], 1.0 op_sel_hi:[1,0]
	v_pk_mul_f32 v[12:13], v[154:155], v[12:13]
	v_pk_add_f32 v[24:25], v[168:169], 1.0 op_sel_hi:[1,0]
	v_pk_fma_f32 v[14:15], v[18:19], v[14:15], v[170:171]
	v_pk_fma_f32 v[18:19], v[22:23], v[10:11], v[174:175]
	v_pk_fma_f32 v[16:17], v[20:21], v[16:17], v[172:173]
	v_pk_fma_f32 v[20:21], v[24:25], v[12:13], v[176:177]
	v_cvt_pk_bf16_f32 v10, v14, v15
	v_cvt_pk_bf16_f32 v11, v16, v17
	v_cvt_pk_bf16_f32 v12, v18, v19
	v_cvt_pk_bf16_f32 v13, v20, v21
	global_store_dwordx4 v[44:45], v[10:13], off
	s_nop 0
	v_pk_mul_f32 v[6:7], v[6:7], v[180:181]
	v_pk_add_f32 v[10:11], v[202:203], 1.0 op_sel_hi:[1,0]
	v_pk_mul_f32 v[2:3], v[2:3], v[198:199]
	v_pk_add_f32 v[14:15], v[210:211], 1.0 op_sel_hi:[1,0]
	v_pk_mul_f32 v[8:9], v[8:9], v[182:183]
	v_pk_add_f32 v[12:13], v[204:205], 1.0 op_sel_hi:[1,0]
	v_pk_mul_f32 v[4:5], v[4:5], v[200:201]
	v_pk_add_f32 v[16:17], v[212:213], 1.0 op_sel_hi:[1,0]
	v_pk_fma_f32 v[6:7], v[6:7], v[10:11], v[214:215]
	v_pk_fma_f32 v[10:11], v[2:3], v[14:15], v[228:229]
	v_pk_fma_f32 v[8:9], v[8:9], v[12:13], v[216:217]
	v_pk_fma_f32 v[12:13], v[4:5], v[16:17], v[230:231]
	v_cvt_pk_bf16_f32 v2, v6, v7
	v_cvt_pk_bf16_f32 v3, v8, v9
	v_cvt_pk_bf16_f32 v4, v10, v11
	v_cvt_pk_bf16_f32 v5, v12, v13
	global_store_dwordx4 v[44:45], v[2:5], off offset:1024
	s_andn2_b64 exec, exec, s[0:1]
	s_cbranch_execz .LBB0_140
